# prep: block-to-work mapping rotated so the 161 small latency-chained blocks are dispatched before the 512 weight-packing blocks
# baseline (speedup 1.0000x reference)
_Z11prep_kernelPKfPDv8_DF16_S0_S0_S0_S0_S0_S0_S0_S0_S0_S2_PfPDF16_S4_S3_:
	s_add_i32 s2, s2, 0x200
	s_cmpk_lt_u32 s2, 0x2a1
	s_cselect_b32 s3, 0, 0x2a1
	s_sub_i32 s2, s2, s3
	s_load_dwordx2 s[16:17], s[0:1], 0x50
	s_cmpk_gt_u32 s2, 0x1ff
	s_mov_b64 s[4:5], -1
	s_cbranch_scc1 .LBB0_3
	s_andn2_b64 vcc, exec, s[4:5]
	s_cbranch_vccz .LBB0_75
